# speedup vs baseline: 1.0265x; 1.0056x over previous
.LBB1_8:
	s_or_b64 exec, exec, s[4:5]
	s_waitcnt vmcnt(1)
	v_mov_b32_e32 v184, 1
	v_lshl_add_u32 v180, v176, 2, v172
	v_lshl_add_u32 v181, v177, 2, v172
	v_lshl_add_u32 v182, v178, 2, v172
	v_lshl_add_u32 v183, v179, 2, v172
	s_waitcnt lgkmcnt(0)
	ds_add_u32 v180, v184
	ds_add_u32 v181, v184
	ds_add_u32 v182, v184
	ds_add_u32 v183, v184
	s_waitcnt lgkmcnt(0)
	ds_read_b32 v151, v173
	s_waitcnt lgkmcnt(0)
	v_cvt_f32_i32_e32 v185, v151
	ds_write_b32 v173, v185 offset:256
	v_add_u32_e32 v10, v172, v2
	s_waitcnt vmcnt(1) lgkmcnt(0)
	s_barrier
	s_nop 0
	s_nop 0
	s_nop 0
	ds_read_b128 v[18:21], v10 offset:256
	ds_read_b128 v[22:25], v10 offset:288
	ds_read_b128 v[82:85], v10 offset:320
	ds_read_b128 v[86:89], v10 offset:352
	ds_read_b128 v[74:77], v10 offset:384
	ds_read_b128 v[78:81], v10 offset:416
	ds_read_b128 v[2:5], v213 offset:32768
	ds_read_b128 v[6:9], v213 offset:0
	ds_read_b128 v[66:69], v10 offset:448
	ds_read_b128 v[70:73], v10 offset:480
	ds_read_b128 v[10:13], v213 offset:1024
	s_waitcnt lgkmcnt(3)
	v_pk_mul_f32 v[26:27], v[8:9], v[20:21]
	v_pk_mul_f32 v[28:29], v[6:7], v[18:19]
	ds_read_b128 v[14:17], v213 offset:8192
	s_waitcnt lgkmcnt(1)
	v_pk_mul_f32 v[12:13], v[12:13], v[24:25]
	v_pk_mul_f32 v[10:11], v[10:11], v[22:23]
	v_pk_fma_f32 v[30:31], v[8:9], v[20:21], v[12:13]
	v_pk_fma_f32 v[32:33], v[6:7], v[18:19], v[10:11]
	v_cvt_pk_bf16_f32 v9, v12, v13
	v_cvt_pk_bf16_f32 v7, v26, v27
	v_cvt_pk_bf16_f32 v8, v10, v11
	v_cvt_pk_bf16_f32 v6, v28, v29
	ds_read_b128 v[10:13], v213 offset:33792
	s_nop 0
	v_mfma_f32_32x32x16_bf16 v[34:49], v[2:5], v[6:9], 0
	ds_read_b128 v[6:9], v213 offset:9216
	s_waitcnt lgkmcnt(2)
	v_mul_f32_e32 v26, v16, v20
	v_mul_f32_e32 v27, v17, v21
	v_pk_mul_f32 v[50:51], v[14:15], v[18:19]
	s_mov_b32 s4, 0x3727c5ac
	s_waitcnt lgkmcnt(0)
	v_pk_mul_f32 v[8:9], v[8:9], v[24:25]
	v_pk_mul_f32 v[28:29], v[6:7], v[22:23]
	v_pk_fma_f32 v[90:91], v[16:17], v[20:21], v[8:9]
	v_pk_fma_f32 v[92:93], v[14:15], v[18:19], v[28:29]
	ds_read_b128 v[14:17], v213 offset:2048
	v_cvt_pk_bf16_f32 v9, v8, v9
	v_cvt_pk_bf16_f32 v7, v26, v27
	v_cvt_pk_bf16_f32 v8, v28, v29
	ds_read_b128 v[26:29], v213 offset:3072
	v_cvt_pk_bf16_f32 v6, v50, v51
	s_waitcnt lgkmcnt(1)
	v_pk_mul_f32 v[94:95], v[14:15], v[82:83]
	s_mov_b32 s0, 0x3c800000
	v_mfma_f32_32x32x16_bf16 v[50:65], v[2:5], v[6:9], 0
	v_mul_f32_e32 v2, v16, v84
	v_mul_f32_e32 v3, v17, v85
	s_waitcnt lgkmcnt(0)
	v_mul_f32_e32 v4, v28, v88
	v_mul_f32_e32 v5, v29, v89
	v_pk_mul_f32 v[6:7], v[26:27], v[86:87]
	v_pk_fma_f32 v[8:9], v[16:17], v[84:85], v[4:5]
	v_cvt_pk_bf16_f32 v3, v2, v3
	v_pk_fma_f32 v[14:15], v[14:15], v[82:83], v[6:7]
	v_pk_add_f32 v[26:27], v[8:9], v[30:31]
	v_cvt_pk_bf16_f32 v5, v4, v5
	v_cvt_pk_bf16_f32 v4, v6, v7
	ds_read_b128 v[6:9], v213 offset:10240
	v_pk_add_f32 v[28:29], v[14:15], v[32:33]
	ds_read_b128 v[14:17], v213 offset:11264
	v_cvt_pk_bf16_f32 v2, v94, v95
	s_waitcnt lgkmcnt(1)
	v_pk_mul_f32 v[30:31], v[6:7], v[82:83]
	v_mov_b64_e32 v[152:153], s[4:5]
	v_mfma_f32_32x32x16_bf16 v[34:49], v[10:13], v[2:5], v[34:49]
	v_mul_f32_e32 v2, v8, v84
	v_mul_f32_e32 v3, v9, v85
	s_waitcnt lgkmcnt(0)
	v_mul_f32_e32 v4, v16, v88
	v_mul_f32_e32 v5, v17, v89
	v_pk_mul_f32 v[14:15], v[14:15], v[86:87]
	v_pk_fma_f32 v[8:9], v[8:9], v[84:85], v[4:5]
	v_pk_fma_f32 v[6:7], v[6:7], v[82:83], v[14:15]
	v_cvt_pk_bf16_f32 v5, v4, v5
	v_cvt_pk_bf16_f32 v3, v2, v3
	v_cvt_pk_bf16_f32 v4, v14, v15
	v_pk_add_f32 v[32:33], v[8:9], v[90:91]
	v_pk_add_f32 v[90:91], v[6:7], v[92:93]
	ds_read_b128 v[6:9], v213 offset:34816
	ds_read_b128 v[14:17], v213 offset:4096
	v_cvt_pk_bf16_f32 v2, v30, v31
	s_mov_b32 s13, 0
	s_mov_b64 s[6:7], 0
	v_mfma_f32_32x32x16_bf16 v[50:65], v[10:13], v[2:5], v[50:65]
	ds_read_b128 v[2:5], v213 offset:5120
	ds_read_b128 v[10:13], v213 offset:12288
	s_waitcnt lgkmcnt(2)
	v_pk_mul_f32 v[30:31], v[16:17], v[76:77]
	v_pk_mul_f32 v[92:93], v[14:15], v[74:75]
	s_waitcnt lgkmcnt(1)
	v_pk_mul_f32 v[4:5], v[4:5], v[80:81]
	v_pk_mul_f32 v[94:95], v[2:3], v[78:79]
	v_pk_fma_f32 v[2:3], v[16:17], v[76:77], v[4:5]
	v_cvt_pk_bf16_f32 v5, v4, v5
	v_pk_add_f32 v[96:97], v[2:3], v[26:27]
	v_cvt_pk_bf16_f32 v3, v30, v31
	v_cvt_pk_bf16_f32 v4, v94, v95
	v_cvt_pk_bf16_f32 v2, v92, v93
	v_pk_fma_f32 v[14:15], v[14:15], v[74:75], v[94:95]
	s_waitcnt lgkmcnt(0)
	v_pk_mul_f32 v[30:31], v[10:11], v[74:75]
	v_mfma_f32_32x32x16_bf16 v[34:49], v[6:9], v[2:5], v[34:49]
	ds_read_b128 v[2:5], v213 offset:13312
	v_add_f32_e32 v98, v14, v28
	v_add_f32_e32 v99, v15, v29
	ds_read_b128 v[14:17], v213 offset:35840
	v_pk_mul_f32 v[26:27], v[12:13], v[76:77]
	s_waitcnt lgkmcnt(1)
	v_pk_mul_f32 v[4:5], v[4:5], v[80:81]
	v_pk_mul_f32 v[28:29], v[2:3], v[78:79]
	v_pk_fma_f32 v[2:3], v[12:13], v[76:77], v[4:5]
	v_pk_fma_f32 v[10:11], v[10:11], v[74:75], v[28:29]
	v_pk_add_f32 v[32:33], v[2:3], v[32:33]
	v_pk_add_f32 v[92:93], v[10:11], v[90:91]
	ds_read_b128 v[10:13], v213 offset:6144
	v_cvt_pk_bf16_f32 v5, v4, v5
	v_cvt_pk_bf16_f32 v3, v26, v27
	v_cvt_pk_bf16_f32 v4, v28, v29
	ds_read_b128 v[26:29], v213 offset:7168
	v_cvt_pk_bf16_f32 v2, v30, v31
	s_waitcnt lgkmcnt(1)
	v_pk_mul_f32 v[30:31], v[10:11], v[66:67]
	v_mfma_f32_32x32x16_bf16 v[50:65], v[6:9], v[2:5], v[50:65]
	v_mul_f32_e32 v2, v12, v68
	v_mul_f32_e32 v3, v13, v69
	s_waitcnt lgkmcnt(0)
	v_mul_f32_e32 v4, v28, v72
	v_mul_f32_e32 v5, v29, v73
	v_pk_mul_f32 v[6:7], v[26:27], v[70:71]
	v_pk_fma_f32 v[8:9], v[12:13], v[68:69], v[4:5]
	v_cvt_pk_bf16_f32 v3, v2, v3
	v_pk_fma_f32 v[10:11], v[10:11], v[66:67], v[6:7]
	v_pk_add_f32 v[94:95], v[8:9], v[96:97]
	v_cvt_pk_bf16_f32 v5, v4, v5
	v_cvt_pk_bf16_f32 v4, v6, v7
	ds_read_b128 v[6:9], v213 offset:14336
	v_pk_add_f32 v[96:97], v[10:11], v[98:99]
	ds_read_b128 v[10:13], v213 offset:15360
	v_cvt_pk_bf16_f32 v2, v30, v31
	s_waitcnt lgkmcnt(1)
	v_pk_mul_f32 v[30:31], v[6:7], v[66:67]
	v_mfma_f32_32x32x16_bf16 v[34:49], v[14:17], v[2:5], v[34:49]
	s_waitcnt lgkmcnt(0)
	v_mul_f32_e32 v10, v10, v70
	v_mul_f32_e32 v11, v11, v71
	v_mul_f32_e32 v2, v8, v68
	v_mul_f32_e32 v3, v9, v69
	v_pk_mul_f32 v[4:5], v[12:13], v[72:73]
	v_pk_fma_f32 v[6:7], v[6:7], v[66:67], v[10:11]
	v_pk_fma_f32 v[8:9], v[8:9], v[68:69], v[4:5]
	v_pk_add_f32 v[92:93], v[6:7], v[92:93]
	v_cvt_pk_bf16_f32 v3, v2, v3
	v_pk_add_f32 v[90:91], v[8:9], v[32:33]
	v_cvt_pk_bf16_f32 v5, v4, v5
	v_cvt_pk_bf16_f32 v4, v10, v11
	ds_read_b128 v[26:29], v213 offset:36864
	ds_read_b128 v[6:9], v213 offset:16384
	v_cvt_pk_bf16_f32 v2, v30, v31
	ds_read_b128 v[98:101], v213 offset:25600
	ds_read_b128 v[102:105], v213 offset:37888
	v_mfma_f32_32x32x16_bf16 v[50:65], v[14:17], v[2:5], v[50:65]
	ds_read_b128 v[2:5], v213 offset:17408
	ds_read_b128 v[30:33], v213 offset:24576
	s_waitcnt lgkmcnt(4)
	v_pk_mul_f32 v[12:13], v[6:7], v[18:19]
	v_pk_mul_f32 v[10:11], v[8:9], v[20:21]
	s_waitcnt lgkmcnt(1)
	v_pk_mul_f32 v[14:15], v[2:3], v[22:23]
	v_pk_mul_f32 v[22:23], v[98:99], v[22:23]
	v_pk_fma_f32 v[112:113], v[6:7], v[18:19], v[14:15]
	s_waitcnt lgkmcnt(0)
	v_pk_mul_f32 v[114:115], v[30:31], v[18:19]
	v_pk_fma_f32 v[118:119], v[30:31], v[18:19], v[22:23]
	v_pk_mul_f32 v[4:5], v[4:5], v[24:25]
	v_pk_mul_f32 v[106:107], v[32:33], v[20:21]
	v_pk_mul_f32 v[24:25], v[100:101], v[24:25]
	ds_read_b128 v[98:101], v213 offset:18432
	v_cvt_pk_bf16_f32 v19, v106, v107
	ds_read_b128 v[106:109], v213 offset:19456
	v_pk_fma_f32 v[110:111], v[8:9], v[20:21], v[4:5]
	v_cvt_pk_bf16_f32 v5, v4, v5
	v_cvt_pk_bf16_f32 v3, v10, v11
	v_cvt_pk_bf16_f32 v4, v14, v15
	s_waitcnt lgkmcnt(0)
	v_pk_mul_f32 v[106:107], v[106:107], v[86:87]
	v_cvt_pk_bf16_f32 v2, v12, v13
	v_pk_mul_f32 v[120:121], v[98:99], v[82:83]
	v_pk_mul_f32 v[108:109], v[108:109], v[88:89]
	v_pk_fma_f32 v[98:99], v[98:99], v[82:83], v[106:107]
	v_mfma_f32_32x32x16_bf16 v[2:17], v[26:29], v[2:5], 0
	v_cvt_pk_bf16_f32 v18, v114, v115
	v_mul_f32_e32 v114, v100, v84
	v_mul_f32_e32 v115, v101, v85
	v_fma_f32 v100, v100, v84, v108
	v_fma_f32 v101, v101, v85, v109
	v_pk_add_f32 v[124:125], v[98:99], v[112:113]
	v_pk_add_f32 v[122:123], v[100:101], v[110:111]
	v_cvt_pk_bf16_f32 v101, v108, v109
	v_cvt_pk_bf16_f32 v100, v106, v107
	ds_read_b128 v[106:109], v213 offset:26624
	v_pk_fma_f32 v[116:117], v[32:33], v[20:21], v[24:25]
	v_cvt_pk_bf16_f32 v21, v24, v25
	v_cvt_pk_bf16_f32 v20, v22, v23
	ds_read_b128 v[110:113], v213 offset:27648
	v_cvt_pk_bf16_f32 v99, v114, v115
	v_mfma_f32_32x32x16_bf16 v[18:33], v[26:29], v[18:21], 0
	v_cvt_pk_bf16_f32 v98, v120, v121
	s_waitcnt lgkmcnt(1)
	v_mul_f32_e32 v114, v106, v82
	v_mul_f32_e32 v115, v107, v83
	s_waitcnt lgkmcnt(0)
	v_pk_mul_f32 v[86:87], v[110:111], v[86:87]
	v_pk_mul_f32 v[88:89], v[112:113], v[88:89]
	v_pk_fma_f32 v[82:83], v[106:107], v[82:83], v[86:87]
	v_mfma_f32_32x32x16_bf16 v[2:17], v[102:105], v[98:101], v[2:17]
	v_mul_f32_e32 v98, v108, v84
	v_mul_f32_e32 v99, v109, v85
	v_fma_f32 v84, v108, v84, v88
	v_fma_f32 v85, v109, v85, v89
	v_add_f32_e32 v108, v82, v118
	v_add_f32_e32 v109, v83, v119
	v_cvt_pk_bf16_f32 v83, v98, v99
	v_pk_add_f32 v[106:107], v[84:85], v[116:117]
	v_cvt_pk_bf16_f32 v85, v88, v89
	v_cvt_pk_bf16_f32 v84, v86, v87
	ds_read_b128 v[86:89], v213 offset:38912
	ds_read_b128 v[98:101], v213 offset:20480
	v_cvt_pk_bf16_f32 v82, v114, v115
	s_waitcnt lgkmcnt(0)
	v_pk_mul_f32 v[110:111], v[100:101], v[76:77]
	v_mfma_f32_32x32x16_bf16 v[18:33], v[102:105], v[82:85], v[18:33]
	ds_read_b128 v[82:85], v213 offset:21504
	ds_read_b128 v[102:105], v213 offset:28672
	v_mul_f32_e32 v112, v98, v74
	v_mul_f32_e32 v113, v99, v75
	s_waitcnt lgkmcnt(1)
	v_pk_mul_f32 v[84:85], v[84:85], v[80:81]
	v_pk_mul_f32 v[114:115], v[82:83], v[78:79]
	v_pk_fma_f32 v[82:83], v[100:101], v[76:77], v[84:85]
	v_cvt_pk_bf16_f32 v85, v84, v85
	v_pk_add_f32 v[116:117], v[82:83], v[122:123]
	v_cvt_pk_bf16_f32 v83, v110, v111
	v_cvt_pk_bf16_f32 v84, v114, v115
	v_cvt_pk_bf16_f32 v82, v112, v113
	v_pk_fma_f32 v[98:99], v[98:99], v[74:75], v[114:115]
	s_waitcnt lgkmcnt(0)
	v_pk_mul_f32 v[112:113], v[102:103], v[74:75]
	v_mfma_f32_32x32x16_bf16 v[2:17], v[86:89], v[82:85], v[2:17]
	ds_read_b128 v[82:85], v213 offset:29696
	v_add_f32_e32 v118, v98, v124
	v_add_f32_e32 v119, v99, v125
	v_mul_f32_e32 v110, v104, v76
	v_mul_f32_e32 v111, v105, v77
	ds_read_b128 v[98:101], v213 offset:39936
	s_waitcnt lgkmcnt(1)
	v_pk_mul_f32 v[78:79], v[82:83], v[78:79]
	v_pk_mul_f32 v[80:81], v[84:85], v[80:81]
	v_pk_fma_f32 v[74:75], v[102:103], v[74:75], v[78:79]
	v_pk_fma_f32 v[76:77], v[104:105], v[76:77], v[80:81]
	v_pk_add_f32 v[104:105], v[74:75], v[108:109]
	v_pk_add_f32 v[102:103], v[76:77], v[106:107]
	v_cvt_pk_bf16_f32 v77, v80, v81
	v_cvt_pk_bf16_f32 v76, v78, v79
	ds_read_b128 v[78:81], v213 offset:22528
	ds_read_b128 v[82:85], v213 offset:23552
	v_cvt_pk_bf16_f32 v75, v110, v111
	v_cvt_pk_bf16_f32 v74, v112, v113
	s_waitcnt lgkmcnt(0)
	v_pk_mul_f32 v[82:83], v[82:83], v[70:71]
	v_mfma_f32_32x32x16_bf16 v[18:33], v[86:89], v[74:77], v[18:33]
	v_mul_f32_e32 v74, v80, v68
	v_mul_f32_e32 v75, v81, v69
	v_mul_f32_e32 v76, v84, v72
	v_mul_f32_e32 v77, v85, v73
	v_mul_f32_e32 v86, v78, v66
	v_mul_f32_e32 v87, v79, v67
	v_pk_fma_f32 v[80:81], v[80:81], v[68:69], v[76:77]
	v_pk_fma_f32 v[78:79], v[78:79], v[66:67], v[82:83]
	v_cvt_pk_bf16_f32 v75, v74, v75
	v_pk_add_f32 v[88:89], v[80:81], v[116:117]
	v_pk_add_f32 v[106:107], v[78:79], v[118:119]
	ds_read_b128 v[78:81], v213 offset:30720
	v_cvt_pk_bf16_f32 v77, v76, v77
	v_cvt_pk_bf16_f32 v76, v82, v83
	ds_read_b128 v[82:85], v213 offset:31744
	v_cvt_pk_bf16_f32 v74, v86, v87
	s_waitcnt lgkmcnt(0)
	v_pk_mul_f32 v[72:73], v[84:85], v[72:73]
	v_mfma_f32_32x32x16_bf16 v[2:17], v[98:101], v[74:77], v[2:17]
	v_mul_f32_e32 v74, v80, v68
	v_mul_f32_e32 v75, v81, v69
	v_fma_f32 v68, v80, v68, v72
	v_fma_f32 v69, v81, v69, v73
	v_mul_f32_e32 v70, v82, v70
	v_mul_f32_e32 v71, v83, v71
	v_pk_add_f32 v[84:85], v[68:69], v[102:103]
	v_cvt_pk_bf16_f32 v69, v72, v73
	v_add_f32_e32 v72, v97, v96
	v_add_f32_e32 v73, v94, v95
	v_pk_mul_f32 v[76:77], v[78:79], v[66:67]
	v_pk_fma_f32 v[66:67], v[78:79], v[66:67], v[70:71]
	v_add_f32_e32 v72, v72, v73
	v_pk_add_f32 v[86:87], v[66:67], v[104:105]
	v_mov_b32_e32 v66, v72
	s_nop 1
	v_permlane32_swap_b32_e32 v72, v66
	v_add_f32_e32 v66, v72, v66
	v_cvt_pk_bf16_f32 v67, v74, v75
	v_rcp_f32_e32 v74, v66
	v_cvt_pk_bf16_f32 v68, v70, v71
	v_cvt_pk_bf16_f32 v66, v76, v77
	v_pk_mul_f32 v[70:71], v[46:47], v[74:75] op_sel_hi:[1,0]
	s_nop 0
	v_mfma_f32_32x32x16_bf16 v[18:33], v[98:101], v[66:69], v[18:33]
	v_mul_f32_e32 v66, v42, v74
	v_mul_f32_e32 v67, v43, v74
	v_add_f32_e32 v42, v93, v92
	v_add_f32_e32 v43, v90, v91
	v_pk_mul_f32 v[68:69], v[44:45], v[74:75] op_sel_hi:[1,0]
	v_add_f32_e32 v42, v42, v43
	v_mov_b32_e32 v43, v42
	s_nop 1
	v_permlane32_swap_b32_e32 v42, v43
	v_add_f32_e32 v42, v42, v43
	v_rcp_f32_e32 v42, v42
	v_add_f32_e32 v44, v107, v106
	v_add_f32_e32 v45, v88, v89
	v_pk_mul_f32 v[72:73], v[48:49], v[74:75] op_sel_hi:[1,0]
	v_add_f32_e32 v44, v44, v45
	v_pk_mul_f32 v[36:37], v[36:37], v[74:75] op_sel_hi:[1,0]
	v_pk_mul_f32 v[38:39], v[38:39], v[74:75] op_sel_hi:[1,0]
	v_pk_mul_f32 v[40:41], v[40:41], v[74:75] op_sel_hi:[1,0]
	v_pk_mul_f32 v[34:35], v[34:35], v[74:75] op_sel_hi:[1,0]
	v_pk_mul_f32 v[74:75], v[58:59], v[42:43] op_sel_hi:[1,0]
	v_pk_mul_f32 v[78:79], v[60:61], v[42:43] op_sel_hi:[1,0]
	v_pk_mul_f32 v[80:81], v[62:63], v[42:43] op_sel_hi:[1,0]
	v_pk_mul_f32 v[82:83], v[64:65], v[42:43] op_sel_hi:[1,0]
	v_pk_mul_f32 v[92:93], v[52:53], v[42:43] op_sel_hi:[1,0]
	v_mov_b32_e32 v43, v44
	s_nop 1
	v_permlane32_swap_b32_e32 v44, v43
	v_add_f32_e32 v43, v44, v43
	v_rcp_f32_e32 v76, v43
	v_pk_mul_f32 v[96:97], v[54:55], v[42:43] op_sel_hi:[1,0]
	v_pk_mul_f32 v[94:95], v[56:57], v[42:43] op_sel_hi:[1,0]
	v_pk_mul_f32 v[98:99], v[50:51], v[42:43] op_sel_hi:[1,0]
	v_pk_mul_f32 v[100:101], v[4:5], v[76:77] op_sel_hi:[1,0]
	v_pk_mov_b32 v[4:5], v[86:87], v[84:85] op_sel:[1,0]
	v_mov_b32_e32 v87, v85
	v_pk_add_f32 v[4:5], v[4:5], v[86:87]
	v_pk_mul_f32 v[102:103], v[6:7], v[76:77] op_sel_hi:[1,0]
	v_pk_add_f32 v[104:105], v[4:5], v[4:5] op_sel:[0,1] op_sel_hi:[1,0]
	v_cvt_pk_bf16_f32 v7, v40, v41
	ds_read_b128 v[84:87], v150 offset:52224
	ds_read_b128 v[50:53], v150 offset:35840
	ds_read_b128 v[54:57], v150 offset:36864
	ds_read_b128 v[58:61], v150 offset:37888
	ds_read_b128 v[62:65], v150 offset:38912
	v_cvt_pk_bf16_f32 v6, v38, v39
	v_cvt_pk_bf16_f32 v5, v36, v37
	v_cvt_pk_bf16_f32 v4, v34, v35
	ds_read_b128 v[88:91], v150 offset:53248
	ds_read_b128 v[34:37], v150 offset:39936
	ds_read_b128 v[38:41], v150 offset:40960
	ds_read_b128 v[42:45], v150 offset:41984
	ds_read_b128 v[46:49], v150 offset:43008
	v_cvt_pk_bf16_f32 v95, v94, v95
	v_cvt_pk_bf16_f32 v94, v96, v97
	v_cvt_pk_bf16_f32 v93, v92, v93
	v_cvt_pk_bf16_f32 v92, v98, v99
	s_waitcnt lgkmcnt(5)
	v_mfma_f32_32x32x16_bf16 v[50:65], v[84:87], v[4:7], v[50:65]
	v_mul_f32_e32 v10, v10, v76
	v_mul_f32_e32 v11, v11, v76
	v_mul_f32_e32 v12, v12, v76
	v_mul_f32_e32 v13, v13, v76
	v_mul_f32_e32 v8, v8, v76
	v_mul_f32_e32 v9, v9, v76
	v_mov_b32_e32 v77, v104
	s_nop 1
	v_permlane32_swap_b32_e32 v104, v77
	v_cvt_pk_bf16_f32 v73, v72, v73
	s_waitcnt lgkmcnt(0)
	v_mfma_f32_32x32x16_bf16 v[34:49], v[84:87], v[92:95], v[34:49]
	v_cvt_pk_bf16_f32 v72, v70, v71
	v_cvt_pk_bf16_f32 v70, v66, v67
	v_add_f32_e32 v66, v104, v77
	v_cvt_pk_bf16_f32 v71, v68, v69
	v_rcp_f32_e32 v104, v66
	v_cvt_pk_bf16_f32 v69, v82, v83
	v_cvt_pk_bf16_f32 v68, v80, v81
	v_cvt_pk_bf16_f32 v67, v78, v79
	v_cvt_pk_bf16_f32 v66, v74, v75
	ds_read_b128 v[78:81], v150 offset:54272
	v_mfma_f32_32x32x16_bf16 v[50:65], v[88:91], v[70:73], v[50:65]
	v_mul_f32_e32 v2, v2, v76
	v_mul_f32_e32 v3, v3, v76
	v_mul_f32_e32 v20, v20, v104
	v_mul_f32_e32 v21, v21, v104
	v_cvt_pk_bf16_f32 v85, v8, v9
	v_cvt_pk_bf16_f32 v82, v2, v3
	v_pk_mul_f32 v[2:3], v[22:23], v[104:105] op_sel_hi:[1,0]
	v_pk_mul_f32 v[8:9], v[24:25], v[104:105] op_sel_hi:[1,0]
	v_pk_mul_f32 v[18:19], v[18:19], v[104:105] op_sel_hi:[1,0]
	v_mfma_f32_32x32x16_bf16 v[34:49], v[88:91], v[66:69], v[34:49]
	v_cvt_pk_bf16_f32 v84, v102, v103
	v_cvt_pk_bf16_f32 v83, v100, v101
	ds_read_b128 v[86:89], v150 offset:55296
	v_cvt_pk_bf16_f32 v99, v8, v9
	v_cvt_pk_bf16_f32 v98, v2, v3
	v_cvt_pk_bf16_f32 v97, v20, v21
	v_cvt_pk_bf16_f32 v96, v18, v19
	s_waitcnt lgkmcnt(1)
	v_mfma_f32_32x32x16_bf16 v[50:65], v[78:81], v[82:85], v[50:65]
	v_mul_f32_e32 v2, v14, v76
	v_mul_f32_e32 v3, v15, v76
	v_mul_f32_e32 v8, v16, v76
	v_mul_f32_e32 v9, v17, v76
	v_mul_f32_e32 v14, v26, v104
	v_mul_f32_e32 v15, v27, v104
	v_cvt_pk_bf16_f32 v77, v8, v9
	v_cvt_pk_bf16_f32 v76, v2, v3
	v_cvt_pk_bf16_f32 v74, v10, v11
	v_pk_mul_f32 v[2:3], v[28:29], v[104:105] op_sel_hi:[1,0]
	v_mfma_f32_32x32x16_bf16 v[34:49], v[78:81], v[96:99], v[34:49]
	v_mul_f32_e32 v8, v30, v104
	v_mul_f32_e32 v9, v31, v104
	v_mul_f32_e32 v10, v32, v104
	v_mul_f32_e32 v11, v33, v104
	v_cvt_pk_bf16_f32 v75, v12, v13
	v_cvt_pk_bf16_f32 v81, v10, v11
	v_cvt_pk_bf16_f32 v80, v8, v9
	v_cvt_pk_bf16_f32 v79, v2, v3
	v_cvt_pk_bf16_f32 v78, v14, v15
	s_waitcnt lgkmcnt(0)
	v_mfma_f32_32x32x16_bf16 v[50:65], v[86:89], v[74:77], v[50:65]
	v_mfma_f32_32x32x16_bf16 v[34:49], v[86:89], v[78:81], v[34:49]
	ds_read_b128 v[86:89], v150 offset:56320
	ds_read_b128 v[18:21], v150 offset:44032
	ds_read_b128 v[22:25], v150 offset:45056
	ds_read_b128 v[26:29], v150 offset:46080
	ds_read_b128 v[30:33], v150 offset:47104
	ds_read_b128 v[100:103], v150 offset:57344
	s_waitcnt lgkmcnt(1)
	v_mfma_f32_32x32x16_bf16 v[18:33], v[86:89], v[4:7], v[18:33]
	ds_read_b128 v[2:5], v150 offset:48128
	ds_read_b128 v[6:9], v150 offset:49152
	ds_read_b128 v[10:13], v150 offset:50176
	ds_read_b128 v[14:17], v150 offset:51200
	s_waitcnt lgkmcnt(0)
	v_mfma_f32_32x32x16_bf16 v[2:17], v[86:89], v[92:95], v[2:17]
	v_mfma_f32_32x32x16_bf16 v[18:33], v[100:103], v[70:73], v[18:33]
	v_mfma_f32_32x32x16_bf16 v[2:17], v[100:103], v[66:69], v[2:17]
	ds_read_b128 v[66:69], v150 offset:58368
	ds_read_b128 v[70:73], v150 offset:59392
	s_waitcnt lgkmcnt(1)
	v_mfma_f32_32x32x16_bf16 v[18:33], v[66:69], v[82:85], v[18:33]
	v_mfma_f32_32x32x16_bf16 v[2:17], v[66:69], v[96:99], v[2:17]
	s_waitcnt lgkmcnt(0)
	v_mfma_f32_32x32x16_bf16 v[18:33], v[70:73], v[74:77], v[18:33]
	v_mfma_f32_32x32x16_bf16 v[2:17], v[70:73], v[78:81], v[2:17]
	s_nop 10
	v_mul_f32_e32 v66, v22, v22
	v_mul_f32_e32 v67, v23, v23
	v_mul_f32_e32 v68, v30, v30
	v_mul_f32_e32 v69, v31, v31
	v_mul_f32_e32 v70, v24, v24
	v_mul_f32_e32 v71, v25, v25
	v_pk_mul_f32 v[72:73], v[32:33], v[32:33]
	v_pk_mul_f32 v[74:75], v[20:21], v[20:21]
	v_pk_mul_f32 v[76:77], v[28:29], v[28:29]
	v_pk_mul_f32 v[78:79], v[26:27], v[26:27]
	v_pk_mul_f32 v[80:81], v[18:19], v[18:19]
	v_pk_fma_f32 v[78:79], v[58:59], v[58:59], v[78:79]
	v_pk_fma_f32 v[76:77], v[60:61], v[60:61], v[76:77]
	v_pk_fma_f32 v[74:75], v[52:53], v[52:53], v[74:75]
	v_pk_fma_f32 v[72:73], v[64:65], v[64:65], v[72:73]
	v_pk_fma_f32 v[70:71], v[56:57], v[56:57], v[70:71]
	v_pk_fma_f32 v[68:69], v[62:63], v[62:63], v[68:69]
	v_pk_fma_f32 v[66:67], v[54:55], v[54:55], v[66:67]
	v_pk_fma_f32 v[80:81], v[50:51], v[50:51], v[80:81]
	v_pk_add_f32 v[66:67], v[66:67], v[68:69]
	v_pk_add_f32 v[68:69], v[70:71], v[72:73]
	v_pk_add_f32 v[70:71], v[74:75], v[76:77]
	v_pk_add_f32 v[72:73], v[80:81], v[78:79]
	v_pk_add_f32 v[68:69], v[70:71], v[68:69]
	v_pk_add_f32 v[66:67], v[72:73], v[66:67]
	v_pk_mul_f32 v[72:73], v[14:15], v[14:15]
	v_pk_mov_b32 v[70:71], v[66:67], v[68:69] op_sel:[1,0]
	v_mov_b32_e32 v67, v69
	v_pk_add_f32 v[66:67], v[70:71], v[66:67]
	v_pk_mul_f32 v[70:71], v[6:7], v[6:7]
	v_pk_mul_f32 v[74:75], v[8:9], v[8:9]
	v_pk_mul_f32 v[76:77], v[16:17], v[16:17]
	v_pk_mul_f32 v[78:79], v[4:5], v[4:5]
	v_pk_mul_f32 v[80:81], v[12:13], v[12:13]
	v_pk_mul_f32 v[82:83], v[10:11], v[10:11]
	v_pk_mul_f32 v[84:85], v[2:3], v[2:3]
	v_pk_fma_f32 v[82:83], v[42:43], v[42:43], v[82:83]
	v_pk_fma_f32 v[80:81], v[44:45], v[44:45], v[80:81]
	v_pk_fma_f32 v[78:79], v[36:37], v[36:37], v[78:79]
	v_pk_fma_f32 v[76:77], v[48:49], v[48:49], v[76:77]
	v_pk_fma_f32 v[74:75], v[40:41], v[40:41], v[74:75]
	v_pk_fma_f32 v[72:73], v[46:47], v[46:47], v[72:73]
	v_pk_fma_f32 v[70:71], v[38:39], v[38:39], v[70:71]
	v_pk_fma_f32 v[84:85], v[34:35], v[34:35], v[84:85]
	v_pk_add_f32 v[70:71], v[70:71], v[72:73]
	v_pk_add_f32 v[72:73], v[74:75], v[76:77]
	v_pk_add_f32 v[74:75], v[78:79], v[80:81]
	v_pk_add_f32 v[76:77], v[84:85], v[82:83]
	v_pk_add_f32 v[72:73], v[74:75], v[72:73]
	v_pk_add_f32 v[70:71], v[76:77], v[70:71]
	v_pk_add_f32 v[66:67], v[66:67], v[66:67] op_sel:[0,1] op_sel_hi:[1,0]
	v_add_f32_e32 v70, v71, v70
	v_add_f32_e32 v71, v72, v73
	v_mov_b32_e32 v69, v66
	v_add_f32_e32 v70, v70, v71
	s_nop 0
	v_permlane32_swap_b32_e32 v66, v69
	v_mov_b32_e32 v68, v70
	s_nop 1
	v_permlane32_swap_b32_e32 v70, v68
	v_mov_b32_e32 v71, v66
	v_pk_add_f32 v[66:67], v[70:71], v[68:69]
	v_pk_fma_f32 v[66:67], v[66:67], s[0:1], v[152:153] op_sel_hi:[1,0,0]
	s_mov_b32 s1, 0x800000
	v_rsq_f32_e32 v68, v67
	s_nop 0
	v_pk_mul_f32 v[158:159], v[50:51], v[68:69] op_sel_hi:[1,0]
	v_pk_mul_f32 v[50:51], v[18:19], v[68:69] op_sel_hi:[1,0]
	v_pk_mul_f32 v[80:81], v[60:61], v[68:69] op_sel_hi:[1,0]
	v_pk_mul_f32 v[60:61], v[28:29], v[68:69] op_sel_hi:[1,0]
	v_pk_mul_f32 v[78:79], v[58:59], v[68:69] op_sel_hi:[1,0]
	v_pk_mul_f32 v[160:161], v[52:53], v[68:69] op_sel_hi:[1,0]
	v_pk_mul_f32 v[82:83], v[54:55], v[68:69] op_sel_hi:[1,0]
	v_rsq_f32_e32 v28, v66
	v_pk_mul_f32 v[168:169], v[56:57], v[68:69] op_sel_hi:[1,0]
	v_pk_mul_f32 v[58:59], v[26:27], v[68:69] op_sel_hi:[1,0]
	v_pk_mul_f32 v[52:53], v[20:21], v[68:69] op_sel_hi:[1,0]
	v_pk_mul_f32 v[54:55], v[22:23], v[68:69] op_sel_hi:[1,0]
	v_pk_mul_f32 v[56:57], v[24:25], v[68:69] op_sel_hi:[1,0]
	v_pk_mul_f32 v[18:19], v[42:43], v[28:29] op_sel_hi:[1,0]
	v_pk_mul_f32 v[20:21], v[44:45], v[28:29] op_sel_hi:[1,0]
	v_pk_mul_f32 v[22:23], v[46:47], v[28:29] op_sel_hi:[1,0]
	v_pk_mul_f32 v[26:27], v[48:49], v[28:29] op_sel_hi:[1,0]
	v_pk_mul_f32 v[162:163], v[34:35], v[28:29] op_sel_hi:[1,0]
	v_pk_mul_f32 v[164:165], v[36:37], v[28:29] op_sel_hi:[1,0]
	v_pk_mul_f32 v[166:167], v[38:39], v[28:29] op_sel_hi:[1,0]
	v_pk_mul_f32 v[24:25], v[40:41], v[28:29] op_sel_hi:[1,0]
	v_pk_mul_f32 v[104:105], v[2:3], v[28:29] op_sel_hi:[1,0]
	v_pk_mul_f32 v[112:113], v[4:5], v[28:29] op_sel_hi:[1,0]
	ds_read_b128 v[2:5], v150 offset:60416
	ds_read_b128 v[34:37], v174 offset:32768
	ds_read_b128 v[38:41], v174 offset:32800
	ds_read_b128 v[42:45], v174 offset:32832
	ds_read_b128 v[46:49], v174 offset:32864
	v_cvt_pk_bf16_f32 v129, v168, v169
	v_cvt_pk_bf16_f32 v128, v82, v83
	v_cvt_pk_bf16_f32 v127, v160, v161
	v_cvt_pk_bf16_f32 v126, v158, v159
	v_cvt_pk_bf16_f32 v137, v24, v25
	v_cvt_pk_bf16_f32 v136, v166, v167
	v_cvt_pk_bf16_f32 v135, v164, v165
	s_waitcnt lgkmcnt(0)
	v_mfma_f32_32x32x16_bf16 v[86:101], v[2:5], v[126:129], v[34:49]
	v_cvt_pk_bf16_f32 v134, v162, v163
	v_mul_f32_e32 v84, v62, v68
	v_mul_f32_e32 v85, v63, v68
	v_mul_f32_e32 v170, v64, v68
	v_mul_f32_e32 v171, v65, v68
	v_pk_mul_f32 v[62:63], v[30:31], v[68:69] op_sel_hi:[1,0]
	v_pk_mul_f32 v[64:65], v[32:33], v[68:69] op_sel_hi:[1,0]
	v_pk_mul_f32 v[116:117], v[6:7], v[28:29] op_sel_hi:[1,0]
	v_pk_mul_f32 v[154:155], v[8:9], v[28:29] op_sel_hi:[1,0]
	v_mfma_f32_32x32x16_bf16 v[34:49], v[2:5], v[134:137], v[34:49]
	ds_read_b128 v[6:9], v150 offset:61440
	ds_read_b128 v[66:69], v174 offset:32896
	ds_read_b128 v[106:109], v150 offset:64512
	v_cvt_pk_bf16_f32 v125, v170, v171
	v_cvt_pk_bf16_f32 v124, v84, v85
	v_cvt_pk_bf16_f32 v123, v80, v81
	v_cvt_pk_bf16_f32 v122, v78, v79
	v_cvt_pk_bf16_f32 v149, v26, v27
	v_cvt_pk_bf16_f32 v148, v22, v23
	v_cvt_pk_bf16_f32 v147, v20, v21
	v_cvt_pk_bf16_f32 v146, v18, v19
	s_waitcnt lgkmcnt(2)
	v_mfma_f32_32x32x16_bf16 v[86:101], v[6:9], v[122:125], v[86:101]
	v_mul_f32_e32 v102, v10, v28
	v_mul_f32_e32 v103, v11, v28
	v_mul_f32_e32 v110, v12, v28
	v_mul_f32_e32 v111, v13, v28
	v_mul_f32_e32 v114, v14, v28
	v_mul_f32_e32 v115, v15, v28
	v_pk_mul_f32 v[156:157], v[16:17], v[28:29] op_sel_hi:[1,0]
	ds_read_b128 v[176:179], v174 offset:33536
	ds_read_b128 v[180:183], v174 offset:33568
	ds_read_b128 v[184:187], v174 offset:33600
	ds_read_b128 v[28:31], v174 offset:33632
	ds_read_b128 v[188:191], v174 offset:33792
	ds_read_b128 v[192:195], v174 offset:33824
	ds_read_b128 v[196:199], v174 offset:33856
	ds_read_b128 v[200:203], v174 offset:33888
	ds_read_b128 v[204:207], v150 offset:62464
	v_cvt_pk_bf16_f32 v133, v56, v57
	v_mfma_f32_32x32x16_bf16 v[34:49], v[6:9], v[146:149], v[34:49]
	v_cvt_pk_bf16_f32 v132, v54, v55
	v_cvt_pk_bf16_f32 v131, v52, v53
	v_cvt_pk_bf16_f32 v130, v50, v51
	ds_read_b128 v[70:73], v174 offset:33664
	ds_read_b128 v[74:77], v174 offset:33920
	ds_read_b128 v[208:211], v150 offset:63488
	v_cvt_pk_bf16_f32 v145, v154, v155
	v_cvt_pk_bf16_f32 v144, v116, v117
	v_cvt_pk_bf16_f32 v143, v112, v113
	v_cvt_pk_bf16_f32 v142, v104, v105
	s_waitcnt lgkmcnt(3)
	v_mfma_f32_32x32x16_bf16 v[86:101], v[204:207], v[130:133], v[86:101]
	v_cvt_pk_bf16_f32 v121, v64, v65
	v_cvt_pk_bf16_f32 v120, v62, v63
	v_cvt_pk_bf16_f32 v119, v60, v61
	v_cvt_pk_bf16_f32 v118, v58, v59
	v_cvt_pk_bf16_f32 v141, v156, v157
	v_cvt_pk_bf16_f32 v140, v114, v115
	v_cvt_pk_bf16_f32 v139, v110, v111
	v_mfma_f32_32x32x16_bf16 v[34:49], v[204:207], v[142:145], v[34:49]
	v_cvt_pk_bf16_f32 v138, v102, v103
	v_fma_f32 v16, v30, v170, v202
	v_fma_f32 v17, v31, v171, v203
	v_fma_f32 v14, v28, v84, v200
	v_fma_f32 v15, v29, v85, v201
	v_pk_fma_f32 v[12:13], v[186:187], v[80:81], v[198:199]
	v_pk_fma_f32 v[10:11], v[184:185], v[78:79], v[196:197]
	v_pk_fma_f32 v[8:9], v[182:183], v[168:169], v[194:195]
	s_waitcnt lgkmcnt(0)
	v_mfma_f32_32x32x16_bf16 v[86:101], v[208:211], v[118:121], v[86:101]
	v_fma_f32 v6, v180, v82, v192
	v_fma_f32 v7, v181, v83, v193
	ds_read_b128 v[78:81], v174 offset:33760
	ds_read_b128 v[82:85], v174 offset:33248
	v_fma_f32 v4, v178, v160, v190
	v_fma_f32 v5, v179, v161, v191
	v_pk_fma_f32 v[2:3], v[176:177], v[158:159], v[188:189]
	v_pk_fma_f32 v[32:33], v[30:31], v[26:27], v[202:203]
	v_pk_fma_f32 v[30:31], v[28:29], v[22:23], v[200:201]
	v_pk_fma_f32 v[28:29], v[186:187], v[20:21], v[198:199]
	v_pk_fma_f32 v[26:27], v[184:185], v[18:19], v[196:197]
	v_pk_fma_f32 v[24:25], v[182:183], v[24:25], v[194:195]
	v_pk_fma_f32 v[22:23], v[180:181], v[166:167], v[192:193]
	v_pk_fma_f32 v[20:21], v[178:179], v[164:165], v[190:191]
	v_pk_fma_f32 v[18:19], v[176:177], v[162:163], v[188:189]
	ds_read_b128 v[158:161], v174 offset:33696
	ds_read_b128 v[162:165], v174 offset:33728
	ds_read_b128 v[166:169], v174 offset:33952
	ds_read_b128 v[176:179], v174 offset:33984
	ds_read_b128 v[180:183], v174 offset:34016
	ds_read_b128 v[184:187], v212 offset:11264
	v_mfma_f32_32x32x16_bf16 v[34:49], v[208:211], v[138:141], v[34:49]
	v_cvt_pk_bf16_f32 v86, v86, v87
	v_cvt_pk_bf16_f32 v87, v88, v89
	v_cvt_pk_bf16_f32 v88, v90, v91
	v_cvt_pk_bf16_f32 v89, v92, v93
	ds_read_b128 v[90:93], v212 offset:12288
	v_pk_max_i16 v86, v86, 0
	v_pk_max_i16 v87, v87, 0
	v_pk_max_i16 v88, v88, 0
	v_pk_max_i16 v89, v89, 0
	s_nop 1
	s_nop 0
	v_cvt_pk_bf16_f32 v188, v34, v35
	v_cvt_pk_bf16_f32 v189, v36, v37
	v_cvt_pk_bf16_f32 v190, v38, v39
	v_cvt_pk_bf16_f32 v191, v40, v41
	s_waitcnt lgkmcnt(1)
	v_mfma_f32_32x32x16_bf16 v[2:17], v[184:187], v[86:89], v[2:17]
	v_pk_max_i16 v188, v188, 0
	v_pk_max_i16 v189, v189, 0
	v_pk_max_i16 v190, v190, 0
	v_pk_max_i16 v191, v191, 0
	v_cvt_pk_bf16_f32 v94, v94, v95
	v_cvt_pk_bf16_f32 v95, v96, v97
	v_cvt_pk_bf16_f32 v96, v98, v99
	v_cvt_pk_bf16_f32 v97, v100, v101
	v_cvt_pk_bf16_f32 v98, v42, v43
	v_cvt_pk_bf16_f32 v99, v44, v45
	v_mfma_f32_32x32x16_bf16 v[18:33], v[184:187], v[188:191], v[18:33]
	ds_read_b128 v[184:187], v212 offset:19456
	v_cvt_pk_bf16_f32 v100, v46, v47
	v_cvt_pk_bf16_f32 v101, v48, v49
	v_fma_f32 v64, v80, v64, v182
	v_fma_f32 v65, v81, v65, v183
	v_pk_fma_f32 v[62:63], v[78:79], v[62:63], v[180:181]
	v_pk_fma_f32 v[60:61], v[164:165], v[60:61], v[178:179]
	v_pk_fma_f32 v[58:59], v[162:163], v[58:59], v[176:177]
	v_pk_max_i16 v94, v94, 0
	v_pk_max_i16 v95, v95, 0
	v_pk_max_i16 v96, v96, 0
	v_pk_max_i16 v97, v97, 0
	v_pk_max_i16 v98, v98, 0
	v_pk_max_i16 v99, v99, 0
	v_pk_max_i16 v100, v100, 0
	v_pk_max_i16 v101, v101, 0
	v_pk_fma_f32 v[56:57], v[160:161], v[56:57], v[168:169]
	s_waitcnt lgkmcnt(1)
	v_mfma_f32_32x32x16_bf16 v[2:17], v[90:93], v[94:97], v[2:17]
	v_fma_f32 v54, v158, v54, v166
	v_fma_f32 v55, v159, v55, v167
	v_fma_f32 v52, v72, v52, v76
	v_fma_f32 v53, v73, v53, v77
	v_fma_f32 v50, v70, v50, v74
	v_fma_f32 v51, v71, v51, v75
	v_pk_fma_f32 v[48:49], v[80:81], v[156:157], v[182:183]
	v_pk_fma_f32 v[46:47], v[78:79], v[114:115], v[180:181]
	v_pk_fma_f32 v[44:45], v[164:165], v[110:111], v[178:179]
	v_pk_fma_f32 v[42:43], v[162:163], v[102:103], v[176:177]
	v_mfma_f32_32x32x16_bf16 v[18:33], v[90:93], v[98:101], v[18:33]
	ds_read_b128 v[90:93], v212 offset:20480
	v_fma_f32 v40, v160, v154, v168
	v_fma_f32 v41, v161, v155, v169
	v_fma_f32 v38, v158, v116, v166
	v_fma_f32 v39, v159, v117, v167
	v_pk_fma_f32 v[36:37], v[72:73], v[112:113], v[76:77]
	v_pk_fma_f32 v[34:35], v[70:71], v[104:105], v[74:75]
	s_waitcnt lgkmcnt(1)
	v_mfma_f32_32x32x16_bf16 v[50:65], v[184:187], v[86:89], v[50:65]
	ds_read_b128 v[70:73], v174 offset:32928
	ds_read_b128 v[74:77], v174 offset:32960
	ds_read_b128 v[78:81], v174 offset:32992
	ds_read_b128 v[86:89], v174 offset:33024
	ds_read_b128 v[110:113], v212 offset:1024
	v_mfma_f32_32x32x16_bf16 v[34:49], v[184:187], v[188:191], v[34:49]
	s_waitcnt lgkmcnt(5)
	v_mfma_f32_32x32x16_bf16 v[50:65], v[90:93], v[94:97], v[50:65]
	v_mfma_f32_32x32x16_bf16 v[34:49], v[90:93], v[98:101], v[34:49]
	s_waitcnt lgkmcnt(2)
	v_mfma_f32_32x32x16_bf16 v[90:105], v[106:109], v[126:129], v[66:81]
	v_mfma_f32_32x32x16_bf16 v[66:81], v[106:109], v[134:137], v[66:81]
	ds_read_b128 v[106:109], v212 offset:0
	s_waitcnt lgkmcnt(0)
	v_mfma_f32_32x32x16_bf16 v[90:105], v[106:109], v[122:125], v[90:105]
	v_mfma_f32_32x32x16_bf16 v[66:81], v[106:109], v[146:149], v[66:81]
	ds_read_b128 v[106:109], v212 offset:2048
	v_mfma_f32_32x32x16_bf16 v[90:105], v[110:113], v[130:133], v[90:105]
	v_mfma_f32_32x32x16_bf16 v[66:81], v[110:113], v[142:145], v[66:81]
	ds_read_b128 v[110:113], v212 offset:13312
	s_waitcnt lgkmcnt(1)
	v_mfma_f32_32x32x16_bf16 v[90:105], v[106:109], v[118:121], v[90:105]
	v_mfma_f32_32x32x16_bf16 v[66:81], v[106:109], v[138:141], v[66:81]
	s_nop 10
	v_cvt_pk_bf16_f32 v90, v90, v91
	v_cvt_pk_bf16_f32 v91, v92, v93
	v_cvt_pk_bf16_f32 v92, v94, v95
	v_cvt_pk_bf16_f32 v94, v98, v99
	v_cvt_pk_bf16_f32 v95, v100, v101
	ds_read_b128 v[98:101], v212 offset:21504
	v_cvt_pk_bf16_f32 v66, v66, v67
	v_cvt_pk_bf16_f32 v67, v68, v69
	v_cvt_pk_bf16_f32 v68, v70, v71
	v_cvt_pk_bf16_f32 v93, v96, v97
	v_cvt_pk_bf16_f32 v69, v72, v73
	ds_read_b128 v[70:73], v212 offset:14336
	v_pk_max_i16 v90, v90, 0
	v_pk_max_i16 v91, v91, 0
	v_pk_max_i16 v92, v92, 0
	v_pk_max_i16 v93, v93, 0
	v_pk_max_i16 v66, v66, 0
	v_pk_max_i16 v67, v67, 0
	v_pk_max_i16 v68, v68, 0
	v_pk_max_i16 v69, v69, 0
	v_cvt_pk_bf16_f32 v96, v102, v103
	s_waitcnt lgkmcnt(2)
	v_mfma_f32_32x32x16_bf16 v[2:17], v[110:113], v[90:93], v[2:17]
	v_cvt_pk_bf16_f32 v97, v104, v105
	v_cvt_pk_bf16_f32 v74, v74, v75
	v_cvt_pk_bf16_f32 v75, v76, v77
	v_cvt_pk_bf16_f32 v76, v78, v79
	v_cvt_pk_bf16_f32 v77, v80, v81
	v_pk_max_i16 v94, v94, 0
	v_pk_max_i16 v95, v95, 0
	v_pk_max_i16 v96, v96, 0
	v_pk_max_i16 v97, v97, 0
	v_pk_max_i16 v74, v74, 0
	v_pk_max_i16 v75, v75, 0
	v_pk_max_i16 v76, v76, 0
	v_pk_max_i16 v77, v77, 0
	v_mfma_f32_32x32x16_bf16 v[18:33], v[110:113], v[66:69], v[18:33]
	s_waitcnt lgkmcnt(1)
	v_mfma_f32_32x32x16_bf16 v[34:49], v[98:101], v[66:69], v[34:49]
	ds_read_b128 v[66:69], v212 offset:22528
	v_mfma_f32_32x32x16_bf16 v[50:65], v[98:101], v[90:93], v[50:65]
	s_waitcnt lgkmcnt(1)
	v_mfma_f32_32x32x16_bf16 v[2:17], v[70:73], v[94:97], v[2:17]
	v_mfma_f32_32x32x16_bf16 v[18:33], v[70:73], v[74:77], v[18:33]
	ds_read_b128 v[78:81], v212 offset:3072
	s_waitcnt lgkmcnt(1)
	v_mfma_f32_32x32x16_bf16 v[50:65], v[66:69], v[94:97], v[50:65]
	ds_read_b128 v[90:93], v174 offset:33056
	ds_read_b128 v[94:97], v174 offset:33088
	ds_read_b128 v[98:101], v174 offset:33120
	ds_read_b128 v[70:73], v174 offset:33152
	v_mfma_f32_32x32x16_bf16 v[34:49], v[66:69], v[74:77], v[34:49]
	ds_read_b128 v[66:69], v212 offset:4096
	ds_read_b128 v[74:77], v212 offset:5120
	s_waitcnt lgkmcnt(3)
	v_mfma_f32_32x32x16_bf16 v[102:117], v[78:81], v[126:129], v[86:101]
	v_mfma_f32_32x32x16_bf16 v[86:101], v[78:81], v[134:137], v[86:101]
	s_waitcnt lgkmcnt(1)
	v_mfma_f32_32x32x16_bf16 v[86:101], v[66:69], v[146:149], v[86:101]
	v_mfma_f32_32x32x16_bf16 v[102:117], v[66:69], v[122:125], v[102:117]
	ds_read_b128 v[66:69], v212 offset:6144
	s_waitcnt lgkmcnt(1)
	v_mfma_f32_32x32x16_bf16 v[86:101], v[74:77], v[142:145], v[86:101]
	v_mfma_f32_32x32x16_bf16 v[102:117], v[74:77], v[130:133], v[102:117]
	ds_read_b128 v[74:77], v212 offset:15360
	s_waitcnt lgkmcnt(1)
	v_mfma_f32_32x32x16_bf16 v[86:101], v[66:69], v[138:141], v[86:101]
	v_mfma_f32_32x32x16_bf16 v[102:117], v[66:69], v[118:121], v[102:117]
	s_nop 10
	v_cvt_pk_bf16_f32 v78, v86, v87
	v_cvt_pk_bf16_f32 v80, v90, v91
	v_cvt_pk_bf16_f32 v79, v88, v89
	v_cvt_pk_bf16_f32 v81, v92, v93
	ds_read_b128 v[86:89], v212 offset:16384
	ds_read_b128 v[90:93], v212 offset:23552
	v_cvt_pk_bf16_f32 v66, v102, v103
	v_cvt_pk_bf16_f32 v67, v104, v105
	v_cvt_pk_bf16_f32 v68, v106, v107
	v_cvt_pk_bf16_f32 v69, v108, v109
	v_pk_max_i16 v66, v66, 0
	v_pk_max_i16 v67, v67, 0
	v_pk_max_i16 v68, v68, 0
	v_pk_max_i16 v69, v69, 0
	v_pk_max_i16 v78, v78, 0
	v_pk_max_i16 v79, v79, 0
	v_pk_max_i16 v80, v80, 0
	v_pk_max_i16 v81, v81, 0
	v_cvt_pk_bf16_f32 v94, v94, v95
	s_waitcnt lgkmcnt(2)
	v_mfma_f32_32x32x16_bf16 v[18:33], v[74:77], v[78:81], v[18:33]
	v_cvt_pk_bf16_f32 v95, v96, v97
	v_cvt_pk_bf16_f32 v96, v98, v99
	v_cvt_pk_bf16_f32 v97, v100, v101
	v_pk_max_i16 v94, v94, 0
	v_pk_max_i16 v95, v95, 0
	v_pk_max_i16 v96, v96, 0
	v_pk_max_i16 v97, v97, 0
	v_mfma_f32_32x32x16_bf16 v[2:17], v[74:77], v[66:69], v[2:17]
	v_cvt_pk_bf16_f32 v74, v110, v111
	v_cvt_pk_bf16_f32 v75, v112, v113
	v_cvt_pk_bf16_f32 v76, v114, v115
	v_cvt_pk_bf16_f32 v77, v116, v117
	v_pk_max_i16 v74, v74, 0
	v_pk_max_i16 v75, v75, 0
	v_pk_max_i16 v76, v76, 0
	v_pk_max_i16 v77, v77, 0
	s_waitcnt lgkmcnt(0)
	v_mfma_f32_32x32x16_bf16 v[50:65], v[90:93], v[66:69], v[50:65]
	ds_read_b128 v[66:69], v212 offset:24576
	v_mfma_f32_32x32x16_bf16 v[34:49], v[90:93], v[78:81], v[34:49]
	ds_read_b128 v[102:105], v212 offset:7168
	v_mfma_f32_32x32x16_bf16 v[2:17], v[86:89], v[74:77], v[2:17]
	s_waitcnt lgkmcnt(1)
	v_mfma_f32_32x32x16_bf16 v[50:65], v[66:69], v[74:77], v[50:65]
	ds_read_b128 v[74:77], v174 offset:33184
	ds_read_b128 v[78:81], v174 offset:33216
	v_mfma_f32_32x32x16_bf16 v[34:49], v[66:69], v[94:97], v[34:49]
	ds_read_b128 v[66:69], v212 offset:8192
	v_mfma_f32_32x32x16_bf16 v[18:33], v[86:89], v[94:97], v[18:33]
	s_waitcnt lgkmcnt(1)
	v_mfma_f32_32x32x16_bf16 v[86:101], v[102:105], v[126:129], v[70:85]
	v_mfma_f32_32x32x16_bf16 v[70:85], v[102:105], v[134:137], v[70:85]
	ds_read_b128 v[102:105], v212 offset:9216
	v_lshlrev_b32_e32 v135, 2, v1
	v_add_u32_e32 v134, v172, v174
	s_waitcnt lgkmcnt(1)
	v_mfma_f32_32x32x16_bf16 v[86:101], v[66:69], v[122:125], v[86:101]
	v_mfma_f32_32x32x16_bf16 v[70:85], v[66:69], v[146:149], v[70:85]
	ds_read_b128 v[66:69], v212 offset:10240
	s_waitcnt lgkmcnt(1)
	v_mfma_f32_32x32x16_bf16 v[86:101], v[102:105], v[130:133], v[86:101]
	v_mfma_f32_32x32x16_bf16 v[70:85], v[102:105], v[142:145], v[70:85]
	ds_read_b128 v[102:105], v212 offset:17408
	s_waitcnt lgkmcnt(1)
	v_mfma_f32_32x32x16_bf16 v[86:101], v[66:69], v[118:121], v[86:101]
	v_mfma_f32_32x32x16_bf16 v[70:85], v[66:69], v[138:141], v[70:85]
	s_nop 10
	v_cvt_pk_bf16_f32 v68, v90, v91
	v_cvt_pk_bf16_f32 v69, v92, v93
	ds_read_b128 v[90:93], v212 offset:25600
	v_cvt_pk_bf16_f32 v66, v86, v87
	v_cvt_pk_bf16_f32 v67, v88, v89
	v_pk_max_i16 v66, v66, 0
	v_pk_max_i16 v67, v67, 0
	v_pk_max_i16 v68, v68, 0
	v_pk_max_i16 v69, v69, 0
	v_cvt_pk_bf16_f32 v70, v70, v71
	v_cvt_pk_bf16_f32 v71, v72, v73
	s_waitcnt lgkmcnt(1)
	v_mfma_f32_32x32x16_bf16 v[2:17], v[102:105], v[66:69], v[2:17]
	v_cvt_pk_bf16_f32 v72, v74, v75
	v_cvt_pk_bf16_f32 v73, v76, v77
	ds_read_b128 v[74:77], v212 offset:18432
	v_cvt_pk_bf16_f32 v86, v94, v95
	v_cvt_pk_bf16_f32 v87, v96, v97
	v_cvt_pk_bf16_f32 v88, v98, v99
	s_waitcnt lgkmcnt(1)
	v_mfma_f32_32x32x16_bf16 v[50:65], v[90:93], v[66:69], v[50:65]
	ds_read_b128 v[66:69], v212 offset:26624
	v_cvt_pk_bf16_f32 v89, v100, v101
	v_pk_max_i16 v86, v86, 0
	v_pk_max_i16 v87, v87, 0
	v_pk_max_i16 v88, v88, 0
	v_pk_max_i16 v89, v89, 0
	v_pk_max_i16 v70, v70, 0
	v_pk_max_i16 v71, v71, 0
	v_pk_max_i16 v72, v72, 0
	v_pk_max_i16 v73, v73, 0
	v_cvt_pk_bf16_f32 v78, v78, v79
	v_cvt_pk_bf16_f32 v79, v80, v81
	s_waitcnt lgkmcnt(1)
	v_mfma_f32_32x32x16_bf16 v[2:17], v[74:77], v[86:89], v[2:17]
	v_cvt_pk_bf16_f32 v80, v82, v83
	v_cvt_pk_bf16_f32 v81, v84, v85
	v_pk_max_i16 v78, v78, 0
	v_pk_max_i16 v79, v79, 0
	v_pk_max_i16 v80, v80, 0
	v_pk_max_i16 v81, v81, 0
	s_waitcnt lgkmcnt(0)
	v_mfma_f32_32x32x16_bf16 v[50:65], v[66:69], v[86:89], v[50:65]
	v_mfma_f32_32x32x16_bf16 v[34:49], v[90:93], v[70:73], v[34:49]
	s_nop 10
	v_add_f32_e32 v130, v10, v58
	v_add_f32_e32 v131, v11, v59
	v_add_f32_e32 v132, v12, v60
	v_add_f32_e32 v133, v13, v61
	v_add_f32_e32 v138, v4, v52
	v_add_f32_e32 v139, v5, v53
	v_pk_add_f32 v[140:141], v[16:17], v[64:65]
	v_pk_add_f32 v[142:143], v[8:9], v[56:57]
	v_pk_add_f32 v[144:145], v[14:15], v[62:63]
	v_pk_add_f32 v[146:147], v[6:7], v[54:55]
	v_mfma_f32_32x32x16_bf16 v[18:33], v[102:105], v[70:73], v[18:33]
	ds_read2st64_b32 v[70:71], v135 offset0:133 offset1:134
	v_add_f32_e32 v148, v2, v50
	v_add_f32_e32 v149, v3, v51
	v_add_f32_e32 v144, v146, v144
	v_add_f32_e32 v145, v147, v145
	v_pk_add_f32 v[140:141], v[142:143], v[140:141]
	v_pk_add_f32 v[132:133], v[138:139], v[132:133]
	v_pk_add_f32 v[130:131], v[148:149], v[130:131]
	v_pk_add_f32 v[132:133], v[132:133], v[140:141]
	v_pk_add_f32 v[130:131], v[130:131], v[144:145]
	v_mfma_f32_32x32x16_bf16 v[34:49], v[66:69], v[78:81], v[34:49]
	s_waitcnt vmcnt(0) lgkmcnt(0)
	v_mul_f32_e32 v66, v175, v70
	v_add_f32_e32 v130, v131, v130
	v_add_f32_e32 v131, v132, v133
	ds_write_b32 v173, v66 offset:512
	v_mul_f32_e32 v66, v175, v71
	v_add_f32_e32 v130, v130, v131
	s_waitcnt lgkmcnt(0)
	ds_read_b128 v[102:105], v174 offset:34560
	ds_read_b128 v[98:101], v174 offset:34592
	ds_read_b128 v[110:113], v174 offset:34624
	ds_read_b128 v[106:109], v174 offset:34656
	ds_read_b128 v[114:117], v174 offset:34688
	ds_read_b128 v[122:125], v174 offset:34720
	ds_read_b128 v[118:121], v174 offset:34752
	ds_read_b128 v[126:129], v174 offset:34784
	v_mov_b32_dpp v66, v66 quad_perm:[1,0,3,2] row_mask:0xf bank_mask:0xf bound_ctrl:1
	v_mov_b32_e32 v131, v130
	v_fmac_f32_e32 v66, v175, v71
	s_nop 0
	v_permlane32_swap_b32_e32 v130, v131
	v_add_f32_dpp v66, v66, v66 quad_perm:[2,3,0,1] row_mask:0xf bank_mask:0xf bound_ctrl:1
	v_add_f32_e32 v130, v130, v131
	v_fmamk_f32 v65, v130, 0xbc800000, v65
	v_add_f32_dpp v66, v66, v66 row_half_mirror row_mask:0xf bank_mask:0xf bound_ctrl:1
	v_fmamk_f32 v64, v130, 0xbc800000, v64
	v_fmamk_f32 v63, v130, 0xbc800000, v63
	v_fmamk_f32 v62, v130, 0xbc800000, v62
	v_fmamk_f32 v61, v130, 0xbc800000, v61
	v_fmamk_f32 v60, v130, 0xbc800000, v60
	v_fmamk_f32 v59, v130, 0xbc800000, v59
	v_fmamk_f32 v58, v130, 0xbc800000, v58
	v_fmamk_f32 v57, v130, 0xbc800000, v57
	v_fmamk_f32 v56, v130, 0xbc800000, v56
	v_fmamk_f32 v55, v130, 0xbc800000, v55
	v_fmamk_f32 v54, v130, 0xbc800000, v54
	v_fmamk_f32 v53, v130, 0xbc800000, v53
	v_fmamk_f32 v52, v130, 0xbc800000, v52
	v_fmamk_f32 v51, v130, 0xbc800000, v51
	v_fmac_f32_e32 v50, 0xbc800000, v130
	v_add_f32_dpp v66, v66, v66 row_ror:8 row_mask:0xf bank_mask:0xf bound_ctrl:1
	v_fmamk_f32 v17, v130, 0xbc800000, v17
	v_fmamk_f32 v16, v130, 0xbc800000, v16
	v_fmamk_f32 v15, v130, 0xbc800000, v15
	v_fmamk_f32 v14, v130, 0xbc800000, v14
	v_fmamk_f32 v13, v130, 0xbc800000, v13
	v_fmamk_f32 v12, v130, 0xbc800000, v12
	v_fmamk_f32 v11, v130, 0xbc800000, v11
	v_fmamk_f32 v10, v130, 0xbc800000, v10
	v_fmamk_f32 v9, v130, 0xbc800000, v9
	v_fmamk_f32 v8, v130, 0xbc800000, v8
	v_fmamk_f32 v7, v130, 0xbc800000, v7
	v_fmamk_f32 v6, v130, 0xbc800000, v6
	v_fmamk_f32 v5, v130, 0xbc800000, v5
	v_fmamk_f32 v4, v130, 0xbc800000, v4
	v_fmamk_f32 v3, v130, 0xbc800000, v3
	v_fmac_f32_e32 v2, 0xbc800000, v130
	v_pk_mul_f32 v[130:131], v[54:55], v[54:55]
	v_pk_mul_f32 v[132:133], v[62:63], v[62:63]
	v_pk_mul_f32 v[138:139], v[50:51], v[50:51]
	v_pk_mul_f32 v[140:141], v[58:59], v[58:59]
	v_pk_mul_f32 v[142:143], v[56:57], v[56:57]
	v_pk_mul_f32 v[144:145], v[64:65], v[64:65]
	v_pk_mul_f32 v[146:147], v[52:53], v[52:53]
	v_pk_mul_f32 v[148:149], v[60:61], v[60:61]
	v_mov_b32_e32 v67, v66
	v_pk_fma_f32 v[148:149], v[12:13], v[12:13], v[148:149]
	v_pk_fma_f32 v[146:147], v[4:5], v[4:5], v[146:147]
	v_pk_fma_f32 v[144:145], v[16:17], v[16:17], v[144:145]
	v_pk_fma_f32 v[142:143], v[8:9], v[8:9], v[142:143]
	v_pk_fma_f32 v[140:141], v[10:11], v[10:11], v[140:141]
	v_pk_fma_f32 v[138:139], v[2:3], v[2:3], v[138:139]
	v_pk_fma_f32 v[132:133], v[14:15], v[14:15], v[132:133]
	v_pk_fma_f32 v[130:131], v[6:7], v[6:7], v[130:131]
	v_permlane16_swap_b32_e32 v66, v67
	v_pk_add_f32 v[130:131], v[130:131], v[132:133]
	v_pk_add_f32 v[132:133], v[138:139], v[140:141]
	v_pk_add_f32 v[138:139], v[142:143], v[144:145]
	v_pk_add_f32 v[140:141], v[146:147], v[148:149]
	v_mfma_f32_32x32x16_bf16 v[18:33], v[74:77], v[78:81], v[18:33]
	v_add_f32_e32 v136, v66, v67
	ds_read_b128 v[70:73], v134 offset:512
	ds_read_b128 v[66:69], v134 offset:544
	ds_read_b128 v[78:81], v134 offset:576
	ds_read_b128 v[74:77], v134 offset:608
	ds_read_b128 v[82:85], v134 offset:640
	ds_read_b128 v[90:93], v134 offset:672
	ds_read_b128 v[86:89], v134 offset:704
	ds_read_b128 v[94:97], v134 offset:736
	v_pk_add_f32 v[138:139], v[140:141], v[138:139]
	v_pk_add_f32 v[130:131], v[132:133], v[130:131]
	s_waitcnt lgkmcnt(8)
	v_pk_mul_f32 v[140:141], v[126:127], v[62:63]
	v_pk_mov_b32 v[132:133], v[130:131], v[138:139] op_sel:[1,0]
	v_mov_b32_e32 v131, v139
	v_pk_mul_f32 v[138:139], v[122:123], v[54:55]
	v_pk_mul_f32 v[142:143], v[114:115], v[50:51]
	v_pk_mul_f32 v[144:145], v[118:119], v[58:59]
	v_pk_mul_f32 v[146:147], v[124:125], v[56:57]
	v_pk_mul_f32 v[148:149], v[128:129], v[64:65]
	v_pk_mul_f32 v[154:155], v[116:117], v[52:53]
	v_pk_mul_f32 v[156:157], v[120:121], v[60:61]
	v_pk_fma_f32 v[154:155], v[104:105], v[4:5], v[154:155]
	v_pk_fma_f32 v[156:157], v[112:113], v[12:13], v[156:157]
	v_pk_fma_f32 v[148:149], v[108:109], v[16:17], v[148:149]
	v_pk_fma_f32 v[146:147], v[100:101], v[8:9], v[146:147]
	v_pk_fma_f32 v[144:145], v[110:111], v[10:11], v[144:145]
	v_pk_fma_f32 v[142:143], v[102:103], v[2:3], v[142:143]
	v_pk_fma_f32 v[140:141], v[106:107], v[14:15], v[140:141]
	v_pk_fma_f32 v[138:139], v[98:99], v[6:7], v[138:139]
	v_pk_add_f32 v[130:131], v[132:133], v[130:131]
	v_pk_add_f32 v[138:139], v[138:139], v[140:141]
	v_pk_add_f32 v[140:141], v[142:143], v[144:145]
	v_pk_add_f32 v[142:143], v[146:147], v[148:149]
	v_pk_add_f32 v[144:145], v[154:155], v[156:157]
	v_pk_add_f32 v[132:133], v[130:131], v[130:131] op_sel:[0,1] op_sel_hi:[1,0]
	v_pk_add_f32 v[142:143], v[144:145], v[142:143]
	v_pk_add_f32 v[138:139], v[140:141], v[138:139]
	v_add_f32_e32 v133, v142, v143
	v_add_f32_e32 v130, v138, v139
	s_waitcnt lgkmcnt(2)
	v_pk_mul_f32 v[138:139], v[90:91], v[54:55]
	s_waitcnt lgkmcnt(0)
	v_pk_mul_f32 v[140:141], v[94:95], v[62:63]
	v_pk_mul_f32 v[142:143], v[82:83], v[50:51]
	v_pk_mul_f32 v[144:145], v[86:87], v[58:59]
	v_pk_mul_f32 v[146:147], v[92:93], v[56:57]
	v_pk_mul_f32 v[148:149], v[96:97], v[64:65]
	v_pk_mul_f32 v[154:155], v[84:85], v[52:53]
	v_pk_mul_f32 v[156:157], v[88:89], v[60:61]
	v_add_f32_e32 v130, v130, v133
	v_pk_fma_f32 v[156:157], v[80:81], v[12:13], v[156:157]
	v_pk_fma_f32 v[154:155], v[72:73], v[4:5], v[154:155]
	v_pk_fma_f32 v[148:149], v[76:77], v[16:17], v[148:149]
	v_pk_fma_f32 v[146:147], v[68:69], v[8:9], v[146:147]
	v_pk_fma_f32 v[144:145], v[78:79], v[10:11], v[144:145]
	v_pk_fma_f32 v[142:143], v[70:71], v[2:3], v[142:143]
	v_pk_fma_f32 v[140:141], v[74:75], v[14:15], v[140:141]
	v_pk_fma_f32 v[138:139], v[66:67], v[6:7], v[138:139]
	v_mov_b32_e32 v133, v130
	v_pk_add_f32 v[138:139], v[138:139], v[140:141]
	v_pk_add_f32 v[140:141], v[142:143], v[144:145]
	v_pk_add_f32 v[142:143], v[146:147], v[148:149]
	v_pk_add_f32 v[144:145], v[154:155], v[156:157]
	v_permlane32_swap_b32_e32 v130, v133
	v_pk_add_f32 v[142:143], v[144:145], v[142:143]
	v_add_f32_e32 v160, v130, v133
	v_pk_add_f32 v[138:139], v[140:141], v[138:139]
	v_add_f32_e32 v133, v142, v143
	v_pk_add_f32 v[140:141], v[26:27], v[42:43]
	v_pk_add_f32 v[142:143], v[28:29], v[44:45]
	v_pk_add_f32 v[144:145], v[20:21], v[36:37]
	v_pk_add_f32 v[146:147], v[32:33], v[48:49]
	v_pk_add_f32 v[148:149], v[24:25], v[40:41]
	v_pk_add_f32 v[154:155], v[30:31], v[46:47]
	v_pk_add_f32 v[156:157], v[22:23], v[38:39]
	v_pk_add_f32 v[158:159], v[18:19], v[34:35]
	v_pk_add_f32 v[154:155], v[156:157], v[154:155]
	v_pk_add_f32 v[146:147], v[148:149], v[146:147]
	v_pk_add_f32 v[142:143], v[144:145], v[142:143]
	v_pk_add_f32 v[140:141], v[158:159], v[140:141]
	v_pk_add_f32 v[142:143], v[142:143], v[146:147]
	v_pk_add_f32 v[140:141], v[140:141], v[154:155]
	v_add_f32_e32 v130, v138, v139
	v_add_f32_e32 v140, v141, v140
	v_add_f32_e32 v141, v142, v143
	v_add_f32_e32 v133, v130, v133
	v_add_f32_e32 v140, v140, v141
	v_mov_b32_e32 v131, v132
	v_mov_b32_e32 v130, v140
	s_nop 1
	v_permlane32_swap_b32_e32 v140, v130
	v_add_f32_e32 v130, v140, v130
	v_fmamk_f32 v49, v130, 0xbc800000, v49
	v_fmamk_f32 v48, v130, 0xbc800000, v48
	v_fmamk_f32 v47, v130, 0xbc800000, v47
	v_fmamk_f32 v46, v130, 0xbc800000, v46
	v_fmamk_f32 v45, v130, 0xbc800000, v45
	v_fmamk_f32 v44, v130, 0xbc800000, v44
	v_fmamk_f32 v43, v130, 0xbc800000, v43
	v_fmamk_f32 v42, v130, 0xbc800000, v42
	v_fmamk_f32 v41, v130, 0xbc800000, v41
	v_fmamk_f32 v40, v130, 0xbc800000, v40
	v_fmamk_f32 v39, v130, 0xbc800000, v39
	v_fmamk_f32 v38, v130, 0xbc800000, v38
	v_fmamk_f32 v37, v130, 0xbc800000, v37
	v_fmamk_f32 v36, v130, 0xbc800000, v36
	v_fmamk_f32 v35, v130, 0xbc800000, v35
	v_fmac_f32_e32 v34, 0xbc800000, v130
	v_fmamk_f32 v33, v130, 0xbc800000, v33
	v_fmamk_f32 v32, v130, 0xbc800000, v32
	v_fmamk_f32 v31, v130, 0xbc800000, v31
	v_fmamk_f32 v30, v130, 0xbc800000, v30
	v_fmamk_f32 v29, v130, 0xbc800000, v29
	v_fmamk_f32 v28, v130, 0xbc800000, v28
	v_fmamk_f32 v27, v130, 0xbc800000, v27
	v_fmamk_f32 v26, v130, 0xbc800000, v26
	v_fmamk_f32 v25, v130, 0xbc800000, v25
	v_fmamk_f32 v24, v130, 0xbc800000, v24
	v_fmamk_f32 v23, v130, 0xbc800000, v23
	v_fmamk_f32 v22, v130, 0xbc800000, v22
	v_fmamk_f32 v21, v130, 0xbc800000, v21
	v_fmamk_f32 v20, v130, 0xbc800000, v20
	v_fmamk_f32 v19, v130, 0xbc800000, v19
	v_fmac_f32_e32 v18, 0xbc800000, v130
	v_pk_mul_f32 v[140:141], v[38:39], v[38:39]
	v_pk_mul_f32 v[142:143], v[46:47], v[46:47]
	v_pk_mul_f32 v[144:145], v[34:35], v[34:35]
	v_pk_mul_f32 v[146:147], v[42:43], v[42:43]
	v_pk_mul_f32 v[148:149], v[40:41], v[40:41]
	v_pk_mul_f32 v[154:155], v[48:49], v[48:49]
	v_pk_mul_f32 v[156:157], v[36:37], v[36:37]
	v_pk_mul_f32 v[158:159], v[44:45], v[44:45]
	v_pk_fma_f32 v[156:157], v[20:21], v[20:21], v[156:157]
	v_pk_fma_f32 v[158:159], v[28:29], v[28:29], v[158:159]
	v_pk_fma_f32 v[154:155], v[32:33], v[32:33], v[154:155]
	v_pk_fma_f32 v[148:149], v[24:25], v[24:25], v[148:149]
	v_pk_fma_f32 v[146:147], v[26:27], v[26:27], v[146:147]
	v_pk_fma_f32 v[144:145], v[18:19], v[18:19], v[144:145]
	v_pk_fma_f32 v[142:143], v[30:31], v[30:31], v[142:143]
	v_pk_fma_f32 v[140:141], v[22:23], v[22:23], v[140:141]
	v_permlane32_swap_b32_e32 v132, v131
	v_pk_add_f32 v[140:141], v[140:141], v[142:143]
	v_pk_add_f32 v[142:143], v[144:145], v[146:147]
	v_pk_add_f32 v[144:145], v[148:149], v[154:155]
	v_pk_add_f32 v[146:147], v[156:157], v[158:159]
	v_pk_add_f32 v[140:141], v[142:143], v[140:141]
	v_pk_add_f32 v[144:145], v[146:147], v[144:145]
	v_pk_mul_f32 v[122:123], v[122:123], v[38:39]
	v_pk_mov_b32 v[142:143], v[140:141], v[144:145] op_sel:[1,0]
	v_mov_b32_e32 v141, v145
	v_pk_add_f32 v[140:141], v[142:143], v[140:141]
	v_pk_mul_f32 v[126:127], v[126:127], v[46:47]
	v_pk_add_f32 v[140:141], v[140:141], v[140:141] op_sel:[0,1] op_sel_hi:[1,0]
	v_pk_mul_f32 v[114:115], v[114:115], v[34:35]
	v_mov_b32_e32 v130, v140
	s_nop 1
	v_permlane32_swap_b32_e32 v140, v130
	v_mov_b32_e32 v141, v132
	v_pk_add_f32 v[130:131], v[140:141], v[130:131]
	v_pk_mul_f32 v[118:119], v[118:119], v[42:43]
	v_pk_fma_f32 v[130:131], v[130:131], s[0:1], v[152:153] op_sel_hi:[1,0,0]
	v_pk_mul_f32 v[124:125], v[124:125], v[40:41]
	v_pk_mul_f32 v[128:129], v[128:129], v[48:49]
	v_pk_mul_f32 v[116:117], v[116:117], v[36:37]
	v_pk_mul_f32 v[120:121], v[120:121], v[44:45]
	v_pk_fma_f32 v[112:113], v[112:113], v[28:29], v[120:121]
	v_pk_fma_f32 v[104:105], v[104:105], v[20:21], v[116:117]
	v_pk_fma_f32 v[108:109], v[108:109], v[32:33], v[128:129]
	v_pk_fma_f32 v[100:101], v[100:101], v[24:25], v[124:125]
	v_pk_fma_f32 v[110:111], v[110:111], v[26:27], v[118:119]
	v_pk_fma_f32 v[102:103], v[102:103], v[18:19], v[114:115]
	v_pk_fma_f32 v[106:107], v[106:107], v[30:31], v[126:127]
	v_pk_fma_f32 v[98:99], v[98:99], v[22:23], v[122:123]
	v_rsq_f32_e32 v131, v131
	v_pk_add_f32 v[98:99], v[98:99], v[106:107]
	v_pk_add_f32 v[102:103], v[102:103], v[110:111]
	v_pk_add_f32 v[100:101], v[100:101], v[108:109]
	v_pk_add_f32 v[104:105], v[104:105], v[112:113]
	v_rsq_f32_e32 v132, v130
	v_pk_add_f32 v[100:101], v[104:105], v[100:101]
	v_pk_add_f32 v[98:99], v[102:103], v[98:99]
	v_add_f32_e32 v98, v98, v99
	v_add_f32_e32 v99, v100, v101
	v_add_f32_e32 v98, v98, v99
	v_mov_b32_e32 v99, v98
	v_pk_mul_f32 v[90:91], v[90:91], v[38:39]
	v_pk_mul_f32 v[94:95], v[94:95], v[46:47]
	v_pk_mul_f32 v[82:83], v[82:83], v[34:35]
	v_pk_mul_f32 v[86:87], v[86:87], v[42:43]
	v_permlane32_swap_b32_e32 v98, v99
	v_pk_fma_f32 v[78:79], v[78:79], v[26:27], v[86:87]
	v_pk_fma_f32 v[70:71], v[70:71], v[18:19], v[82:83]
	v_pk_fma_f32 v[74:75], v[74:75], v[30:31], v[94:95]
	v_pk_fma_f32 v[66:67], v[66:67], v[22:23], v[90:91]
	v_mov_b32_e32 v130, v131
	v_mov_b32_e32 v131, v132
	v_add_f32_e32 v98, v98, v99
	v_pk_add_f32 v[66:67], v[66:67], v[74:75]
	v_pk_add_f32 v[70:71], v[70:71], v[78:79]
	v_mul_f32_e32 v139, v160, v130
	v_mul_f32_e32 v98, v98, v131
	v_pk_add_f32 v[66:67], v[70:71], v[66:67]
	v_cmp_gt_u32_e32 vcc, 32, v1
	v_add_f32_e32 v66, v66, v67
	v_pk_mul_f32 v[92:93], v[92:93], v[40:41]
	v_cndmask_b32_e32 v67, v98, v139, vcc
	v_add_f32_e32 v67, s12, v67
	v_pk_mul_f32 v[96:97], v[96:97], v[48:49]
	v_pk_mul_f32 v[84:85], v[84:85], v[36:37]
	v_pk_mul_f32 v[88:89], v[88:89], v[44:45]
	v_mul_f32_e32 v67, 0xbfb8aa3b, v67
	v_pk_fma_f32 v[80:81], v[80:81], v[28:29], v[88:89]
	v_pk_fma_f32 v[72:73], v[72:73], v[20:21], v[84:85]
	v_pk_fma_f32 v[76:77], v[76:77], v[32:33], v[96:97]
	v_pk_fma_f32 v[68:69], v[68:69], v[24:25], v[92:93]
	v_exp_f32_e32 v70, v67
	v_pk_add_f32 v[68:69], v[68:69], v[76:77]
	v_pk_add_f32 v[72:73], v[72:73], v[80:81]
	v_cmp_lt_i32_e64 s[0:1], 0, v151
	v_pk_add_f32 v[68:69], v[72:73], v[68:69]
	v_mov_b32_e32 v137, v136
	v_add_f32_e32 v67, v68, v69
	v_add_f32_e32 v67, v66, v67
	v_add_f32_e32 v66, 1.0, v70
	v_rcp_f32_e32 v66, v66
	v_mov_b32_e32 v69, 0xff800000
	v_mov_b32_e32 v138, v133
	v_mov_b32_e32 v68, v67
	v_cndmask_b32_e64 v70, v69, v66, s[0:1]
	v_mbcnt_lo_u32_b32 v66, -1, 0
	v_mbcnt_hi_u32_b32 v66, -1, v66
	v_permlane32_swap_b32_e32 v136, v137
	v_permlane32_swap_b32_e32 v133, v138
	v_permlane32_swap_b32_e32 v67, v68
	v_and_b32_e32 v86, 64, v66
	s_mov_b32 s14, 8
	s_mov_b32 s13, 0
	v_mov_b32_e32 v66, 0
	s_waitcnt lgkmcnt(0)
